# v46 + code placement (9.3): one s_nop 0 at P4 entry shifts P4..P9 by 4 bytes back to the baseline's MFMA byte phase
# speedup vs baseline: 1.0034x; 1.0034x over previous
; #define SEAM(k) do { if (IN(k) && IN((k) + 1)) xcd_barrier(bar); } while (0)
;     __device__ __forceinline__ bool next(int i, Unit& u) const {
;         if (i >= 2 || c >= 256) return false;
;         int pm, pn; static_tile(c, 32, 8, pm, pn);
; __global__ void __launch_bounds__(512, 2) fwd(Args args) {
;     ...
;     if (IN(4)) { MergeOrder S{(int)blockIdx.x, (const char*)(F.ws + WS_ONA), (const char*)(F.ws + WS_ODF), (const char*)(F.ws + WS_WPNAT), (const char*)(F.ws + WS_WPDFT)};
;         EpiMerge E{(const bf16_t*)(F.ws + WS_GNA), (const bf16_t*)(F.ws + WS_GDF), F.ws + WS_YP8, F.lds + TAB_OFF};
;         pg8::gemm_phase<EpiMerge, MergeOrder, false, true>(F.lds, 512, S, E); } SEAM(4);
.LBB0_542:
	s_nop 0
	s_cmp_lt_i32 s34, 5
	s_cselect_b64 s[16:17], -1, 0
	s_and_b64 s[0:1], s[16:17], s[0:1]
	v_cndmask_b32_e64 v1, 0, 1, s[12:13]
	s_andn2_b64 vcc, exec, s[0:1]
	v_cmp_ne_u32_e64 s[0:1], 1, v1
	s_cbranch_vccnz .LBB0_643
	s_and_b64 vcc, exec, s[0:1]
	v_readfirstlane_b32 s6, v0
	s_cbranch_vccnz .LBB0_546
	s_ashr_i32 s3, s2, 31
	s_lshr_b32 s3, s3, 29
	s_add_i32 s3, s2, s3
	s_and_b32 s4, s3, -8
	s_sub_i32 s7, s2, s4
	s_cmp_gt_i32 s7, -1
	s_cbranch_scc0 .LBB0_547
	s_lshl_b32 s12, s7, 5
	s_cbranch_execz .LBB0_548
	s_branch .LBB0_549
